# mixer work queues: next unit index drawn ahead of time (attention: at the start of the unit epilogue; mLSTM-out: one unit ahead) so the atomic latency overlaps with work
# speedup vs baseline: 1.0036x; 1.0036x over previous
; __device__ __forceinline__ int crow(int r,int hi){return (r&3)+8*(r>>2)+4*hi;}
; template<int THRL> __device__ __forceinline__ void attn_unit(int b,int h,int qb,const bf16*Q,const bf16*__restrict__ K,const bf16*__restrict__ V,bf16*O,const float*__restrict__ F2g,const float*__restrict__ gain,float qkb,char*shm){
;     ...
;   {auto rr=__builtin_amdgcn_permlane32_swap(__float_as_uint(l_reg),__float_as_uint(l_reg),false,false);l_reg=__uint_as_float(rr[0])+__uint_as_float(rr[1]);}
;   if(hi==0)wsf[32+r32]=l_reg;asm volatile("s_waitcnt lgkmcnt(0)":::"memory");
;   float rli[16];
;   #pragma unroll
;   for(int r=0;r<16;++r)rli[r]=__builtin_amdgcn_rcpf(wsf[32+crow(r,hi)]);
;   bf16*Ow=O+(rowbase+q0+wid*QBLK)*DO+h*D;
;   { bf16*stg=(bf16*)(shm+LDS_OST)+wid*2048;
;     #pragma unroll
;     for(int r=0;r<16;++r){const int orow=crow(r,hi);
;       #pragma unroll
;       for(int d0=0;d0<2;++d0)stg[orow*64+d0*32+r32]=__float2bfloat16(o[d0][r]*rli[r]);}
;     asm volatile("s_waitcnt lgkmcnt(0)":::"memory");
;     const f32x4_t g0=*(const f32x4_t*)(gain+h*D+(lane&7)*8), g1=*(const f32x4_t*)(gain+h*D+(lane&7)*8+4);
;     #pragma unroll
;     for(int i=0;i<4;++i){const int row=i*8+(lane>>3),ch=lane&7; const u32x4 v=*(const u32x4*)(stg+row*64+ch*8);
; __global__ void __launch_bounds__(NWAVES * 64, 2) mega_fwd(Args args) {
;     ...
;             for (int pa_ = 0; pa_ <= PROBE_ATT2; ++pa_) for (;;) {
;                 if (F.tid == 0) QS[0] = (int)__hip_atomic_fetch_add(F.ctl + CW_Q + 64 * F.l + 4 * pa_, 1u, __ATOMIC_RELAXED, __HIP_MEMORY_SCOPE_AGENT);
;                 __syncthreads();
;                 const int idx = __builtin_amdgcn_readfirstlane(QS[0]);
.LBB0_2750:
	s_add_u32 s37, s10, 0xb100000
	s_addc_u32 s38, s11, 0
	s_add_u32 s39, s10, 0xb100200
	s_addc_u32 s40, s11, 0
	s_add_u32 s41, s10, 0xb100400
	s_addc_u32 s42, s11, 0
	s_add_u32 s43, s10, 0x18100000
	s_addc_u32 s44, s11, 0
	s_add_u32 s45, s10, 0x200000
	s_addc_u32 s47, s11, 0
	s_lshl_b64 s[18:19], s[8:9], 12
	s_add_u32 s9, s1, s18
	s_addc_u32 s46, s46, s19
	s_ashr_i32 s1, s0, 31
	s_lshl_b64 s[0:1], s[0:1], 2
	s_add_u32 s0, s10, s0
	s_addc_u32 s1, s11, s1
	s_add_u32 s6, s0, 0x8000
	s_addc_u32 s7, s1, 0
	s_lshl_b32 s0, s8, 6
	s_ashr_i32 s1, s0, 31
	s_add_i32 s17, s17, 0x20280
	s_lshl_b64 s[12:13], s[0:1], 2
	s_add_u32 s0, s10, s12
	s_addc_u32 s1, s11, s13
	s_add_u32 s22, s0, 0x9000
	v_cmp_eq_u32_e64 s[2:3], 0, v130
	s_addc_u32 s23, s1, 0
	s_and_saveexec_b64 s[62:63], s[2:3]
	v_mov_b32_e32 v201, 1
	global_atomic_add v200, v3, v201, s[22:23] sc0
	s_mov_b64 exec, s[62:63]
	s_branch .LBB0_2753
.LBB0_2751:
	s_or_b64 exec, exec, s[0:1]
	s_and_saveexec_b64 s[62:63], s[2:3]
	v_mov_b32_e32 v201, 1
	global_atomic_add v200, v3, v201, s[22:23] sc0
	s_mov_b64 exec, s[62:63]
	s_waitcnt lgkmcnt(0)
	ds_read_b128 v[4:7], v1 offset:49280
	ds_read_b128 v[8:11], v1 offset:49312
	s_lshl_b64 s[0:1], s[24:25], 11
	s_add_u32 s0, s43, s0
	s_addc_u32 s1, s44, s1
	s_waitcnt lgkmcnt(1)
	v_rcp_f32_e32 v2, v4
	v_rcp_f32_e32 v12, v5
	v_rcp_f32_e32 v13, v6
	v_rcp_f32_e32 v14, v7
	ds_read_b128 v[4:7], v1 offset:49344
	s_lshl_b32 s4, s51, 12
	s_add_i32 s24, s4, 0
	v_lshlrev_b32_e32 v0, 1, v0
	s_waitcnt lgkmcnt(1)
	v_rcp_f32_e32 v8, v8
	s_waitcnt lgkmcnt(0)
	v_rcp_f32_e32 v15, v4
	v_rcp_f32_e32 v16, v5
	v_rcp_f32_e32 v17, v6
	v_rcp_f32_e32 v50, v7
	ds_read_b128 v[4:7], v1 offset:49376
	v_rcp_f32_e32 v9, v9
	v_rcp_f32_e32 v10, v10
	v_rcp_f32_e32 v11, v11
	s_lshl_b32 s4, s59, 1
	s_waitcnt lgkmcnt(0)
	v_rcp_f32_e32 v1, v4
	v_rcp_f32_e32 v4, v5
	v_rcp_f32_e32 v5, v6
	v_rcp_f32_e32 v6, v7
	v_lshlrev_b32_e32 v7, 9, v217
	v_add3_u32 v0, s24, v0, v7
	v_mul_f32_e32 v7, v34, v2
	v_mul_f32_e32 v2, v18, v2
	v_cvt_pk_bf16_f32 v2, v2, s0
	ds_write_b16 v0, v2 offset:51264
	v_mul_f32_e32 v2, v35, v12
	v_cvt_pk_bf16_f32 v2, v2, s0
	ds_write_b16 v0, v2 offset:51328
	v_mul_f32_e32 v2, v19, v12
	v_cvt_pk_bf16_f32 v2, v2, s0
	ds_write_b16 v0, v2 offset:51392
	v_mul_f32_e32 v2, v36, v13
	v_cvt_pk_bf16_f32 v2, v2, s0
	ds_write_b16 v0, v2 offset:51456
	v_mul_f32_e32 v2, v20, v13
	v_cvt_pk_bf16_f32 v2, v2, s0
	ds_write_b16 v0, v2 offset:51520
	v_mul_f32_e32 v2, v37, v14
	v_cvt_pk_bf16_f32 v2, v2, s0
	ds_write_b16 v0, v2 offset:51584
	v_mul_f32_e32 v2, v21, v14
	v_cvt_pk_bf16_f32 v2, v2, s0
	ds_write_b16 v0, v2 offset:51648
	v_mul_f32_e32 v2, v38, v8
	v_cvt_pk_bf16_f32 v2, v2, s0
	ds_write_b16 v0, v2 offset:52224
	v_mul_f32_e32 v2, v22, v8
	v_cvt_pk_bf16_f32 v2, v2, s0
	ds_write_b16 v0, v2 offset:52288
	v_mul_f32_e32 v2, v39, v9
	v_cvt_pk_bf16_f32 v2, v2, s0
	ds_write_b16 v0, v2 offset:52352
	v_mul_f32_e32 v2, v23, v9
	v_cvt_pk_bf16_f32 v2, v2, s0
	ds_write_b16 v0, v2 offset:52416
	v_mul_f32_e32 v2, v40, v10
	v_cvt_pk_bf16_f32 v2, v2, s0
	ds_write_b16 v0, v2 offset:52480
	v_mul_f32_e32 v2, v24, v10
	v_cvt_pk_bf16_f32 v2, v2, s0
	ds_write_b16 v0, v2 offset:52544
	v_mul_f32_e32 v2, v41, v11
	v_cvt_pk_bf16_f32 v2, v2, s0
	ds_write_b16 v0, v2 offset:52608
	v_mul_f32_e32 v2, v25, v11
	v_cvt_pk_bf16_f32 v2, v2, s0
	ds_write_b16 v0, v2 offset:52672
	v_mul_f32_e32 v2, v42, v15
	v_cvt_pk_bf16_f32 v2, v2, s0
	ds_write_b16 v0, v2 offset:53248
	v_mul_f32_e32 v2, v26, v15
	v_cvt_pk_bf16_f32 v2, v2, s0
	ds_write_b16 v0, v2 offset:53312
	v_mul_f32_e32 v2, v43, v16
	v_cvt_pk_bf16_f32 v2, v2, s0
	ds_write_b16 v0, v2 offset:53376
	v_mul_f32_e32 v2, v27, v16
	v_cvt_pk_bf16_f32 v2, v2, s0
	ds_write_b16 v0, v2 offset:53440
	v_mul_f32_e32 v2, v44, v17
	v_cvt_pk_bf16_f32 v2, v2, s0
	ds_write_b16 v0, v2 offset:53504
	v_mul_f32_e32 v2, v28, v17
	v_cvt_pk_bf16_f32 v2, v2, s0
	ds_write_b16 v0, v2 offset:53568
	v_mul_f32_e32 v2, v45, v50
	v_cvt_pk_bf16_f32 v2, v2, s0
	ds_write_b16 v0, v2 offset:53632
	v_mul_f32_e32 v2, v29, v50
	v_cvt_pk_bf16_f32 v2, v2, s0
	ds_write_b16 v0, v2 offset:53696
	v_mul_f32_e32 v2, v46, v1
	v_mul_f32_e32 v1, v30, v1
	v_cvt_pk_bf16_f32 v1, v1, s0
	ds_write_b16 v0, v1 offset:54336
	v_mul_f32_e32 v1, v47, v4
	v_cvt_pk_bf16_f32 v1, v1, s0
	ds_write_b16 v0, v1 offset:54400
	v_mul_f32_e32 v1, v31, v4
	v_cvt_pk_bf16_f32 v1, v1, s0
	ds_write_b16 v0, v1 offset:54464
	v_mul_f32_e32 v1, v48, v5
	v_cvt_pk_bf16_f32 v1, v1, s0
	ds_write_b16 v0, v1 offset:54528
	v_mul_f32_e32 v1, v32, v5
	v_cvt_pk_bf16_f32 v1, v1, s0
	ds_write_b16 v0, v1 offset:54592
	v_mul_f32_e32 v1, v49, v6
	v_cvt_pk_bf16_f32 v1, v1, s0
	ds_write_b16 v0, v1 offset:54656
	v_mul_f32_e32 v1, v33, v6
	v_cvt_pk_bf16_f32 v7, v7, s0
	v_cvt_pk_bf16_f32 v2, v2, s0
	v_cvt_pk_bf16_f32 v1, v1, s0
	s_add_u32 s0, s0, s4
	s_addc_u32 s1, s1, 0
	s_lshl_b32 s4, s59, 2
	ds_write_b16 v0, v7 offset:51200
	ds_write_b16 v0, v2 offset:54272
	ds_write_b16 v0, v1 offset:54720
	s_add_u32 s4, s9, s4
	v_and_b32_e32 v0, 56, v223
	s_waitcnt lgkmcnt(0)
	s_addc_u32 s5, s46, 0
	v_lshlrev_b32_e32 v1, 2, v0
	global_load_dwordx4 v[4:7], v1, s[4:5] offset:16
	global_load_dwordx4 v[8:11], v1, s[4:5]
	v_lshlrev_b32_e32 v2, 1, v0
	v_lshrrev_b32_e32 v52, 3, v131
	v_add_u32_e32 v53, s24, v2
	v_lshlrev_b32_e32 v0, 2, v131
	v_xor_b32_e32 v25, 4, v0
	v_xor_b32_e32 v24, 8, v0
	v_xor_b32_e32 v1, 16, v0
	v_lshl_add_u32 v0, v52, 7, v53
	ds_read_b128 v[14:17], v0 offset:51200
	v_lshl_add_u64 v[12:13], s[0:1], 0, v[2:3]
	v_lshlrev_b32_e32 v2, 11, v52
	v_lshl_add_u64 v[36:37], v[12:13], 0, v[2:3]
	v_or_b32_e32 v2, 8, v52
	v_lshl_add_u32 v0, v2, 7, v53
	s_waitcnt lgkmcnt(0)
; __device__ __forceinline__ unsigned cvtpk_s(float lo,float hi){f32x2_t v={lo,hi};bf16x2_t b=__builtin_convertvector(v,bf16x2_t);return __builtin_bit_cast(unsigned,b);}
; template<int THRL> __device__ __forceinline__ void attn_unit(int b,int h,int qb,const bf16*Q,const bf16*__restrict__ K,const bf16*__restrict__ V,bf16*O,const float*__restrict__ F2g,const float*__restrict__ gain,float qkb,char*shm){
;     ...
;     for(int i=0;i<4;++i){const int row=i*8+(lane>>3),ch=lane&7; const u32x4 v=*(const u32x4*)(stg+row*64+ch*8);
;       float x[8];
;       #pragma unroll
;       for(int e=0;e<4;++e){ x[2*e]=__uint_as_float(v[e]<<16); x[2*e+1]=__uint_as_float(v[e]&0xffff0000u); }
;       float ss=0.f;
;       #pragma unroll
;       for(int e=0;e<8;++e)ss+=x[e]*x[e];
;       ss+=__int_as_float(__builtin_amdgcn_ds_bpermute((lane^1)<<2,__float_as_int(ss))); ss+=__int_as_float(__builtin_amdgcn_ds_bpermute((lane^2)<<2,__float_as_int(ss))); ss+=__int_as_float(__builtin_amdgcn_ds_bpermute((lane^4)<<2,__float_as_int(ss)));
;       const float rs=rsqrtf(ss*(1.0f/64.0f)+1e-6f);
;       u32x4 w; w[0]=cvtpk_s(x[0]*rs*g0[0],x[1]*rs*g0[1]); w[1]=cvtpk_s(x[2]*rs*g0[2],x[3]*rs*g0[3]); w[2]=cvtpk_s(x[4]*rs*g1[0],x[5]*rs*g1[1]); w[3]=cvtpk_s(x[6]*rs*g1[2],x[7]*rs*g1[3]);
;       ATTN_STORE16(Ow+(long)row*DO+ch*8,w);} }
	v_lshlrev_b32_e32 v20, 16, v17
	v_and_b32_e32 v21, 0xffff0000, v17
	v_lshlrev_b32_e32 v22, 16, v16
	v_and_b32_e32 v23, 0xffff0000, v16
	v_lshlrev_b32_e32 v28, 16, v15
	v_and_b32_e32 v29, 0xffff0000, v15
	v_lshlrev_b32_e32 v32, 16, v14
	v_and_b32_e32 v33, 0xffff0000, v14
	ds_read_b128 v[14:17], v0 offset:51200
	v_pk_mul_f32 v[34:35], v[32:33], v[32:33]
	v_pk_mul_f32 v[30:31], v[28:29], v[28:29]
	v_mov_b32_e32 v51, v34
	v_pk_mul_f32 v[26:27], v[22:23], v[22:23]
	s_waitcnt lgkmcnt(0)
	v_lshlrev_b32_e32 v48, 16, v14
	v_and_b32_e32 v49, 0xffff0000, v14
	v_lshlrev_b32_e32 v44, 16, v15
	v_and_b32_e32 v45, 0xffff0000, v15
	v_pk_mul_f32 v[14:15], v[48:49], v[48:49]
	v_pk_mul_f32 v[46:47], v[44:45], v[44:45]
	v_mov_b32_e32 v50, v14
	v_mov_b32_e32 v34, v15
	v_lshlrev_b32_e32 v42, 16, v16
	v_and_b32_e32 v43, 0xffff0000, v16
	v_pk_add_f32 v[14:15], v[50:51], v[34:35]
	v_mov_b32_e32 v34, v46
	v_mov_b32_e32 v35, v30
	v_lshlrev_b32_e32 v38, 16, v17
	v_and_b32_e32 v39, 0xffff0000, v17
	v_pk_mul_f32 v[16:17], v[42:43], v[42:43]
	v_pk_add_f32 v[14:15], v[34:35], v[14:15]
	v_mov_b32_e32 v30, v47
	v_pk_add_f32 v[14:15], v[30:31], v[14:15]
	v_mov_b32_e32 v30, v16
	v_mov_b32_e32 v31, v26
	v_pk_mul_f32 v[18:19], v[20:21], v[20:21]
	v_pk_mul_f32 v[40:41], v[38:39], v[38:39]
	v_pk_add_f32 v[14:15], v[30:31], v[14:15]
	v_mov_b32_e32 v26, v17
	v_pk_add_f32 v[14:15], v[26:27], v[14:15]
	v_mov_b32_e32 v16, v40
	v_mov_b32_e32 v17, v18
	v_pk_add_f32 v[14:15], v[16:17], v[14:15]
	v_mov_b32_e32 v18, v41
	v_pk_add_f32 v[14:15], v[18:19], v[14:15]
	ds_bpermute_b32 v17, v25, v15
	ds_bpermute_b32 v16, v25, v14
	s_mov_b32 s0, 0x358637bd
	v_lshlrev_b32_e32 v2, 11, v2
	v_or_b32_e32 v54, 24, v52
	v_mov_b32_e32 v216, 0x3ecc95a3
	s_waitcnt lgkmcnt(0)
	v_pk_add_f32 v[14:15], v[14:15], v[16:17]
	ds_bpermute_b32 v17, v24, v15
	ds_bpermute_b32 v16, v24, v14
	s_waitcnt lgkmcnt(0)
	v_pk_add_f32 v[14:15], v[14:15], v[16:17]
	ds_bpermute_b32 v17, v1, v15
	ds_bpermute_b32 v16, v1, v14
	s_waitcnt lgkmcnt(0)
	v_pk_add_f32 v[16:17], v[14:15], v[16:17]
	v_mov_b64_e32 v[14:15], s[0:1]
	v_pk_fma_f32 v[26:27], v[16:17], s[96:97], v[14:15] op_sel_hi:[1,0,0]
	s_nop 0
	v_mul_f32_e32 v0, 0x4b800000, v27
	v_cmp_gt_f32_e64 s[0:1], s83, v27
	v_cmp_gt_f32_e32 vcc, s83, v26
	s_nop 0
	v_cndmask_b32_e64 v0, v27, v0, s[0:1]
	v_rsq_f32_e32 v0, v0
	s_nop 0
	v_mul_f32_e32 v16, 0x45800000, v0
	v_cndmask_b32_e64 v0, v0, v16, s[0:1]
	v_pk_mul_f32 v[16:17], v[0:1], v[32:33] op_sel_hi:[0,1]
	v_pk_mul_f32 v[18:19], v[0:1], v[28:29] op_sel_hi:[0,1]
	s_waitcnt vmcnt(0)
	v_pk_mul_f32 v[16:17], v[8:9], v[16:17]
	v_pk_mul_f32 v[18:19], v[10:11], v[18:19]
	v_cvt_pk_bf16_f32 v16, v16, v17
	v_cvt_pk_bf16_f32 v17, v18, v19
	v_pk_mul_f32 v[18:19], v[0:1], v[22:23] op_sel_hi:[0,1]
	v_pk_mul_f32 v[20:21], v[0:1], v[20:21] op_sel_hi:[0,1]
	v_mul_f32_e32 v0, 0x4b800000, v26
	v_cndmask_b32_e32 v0, v26, v0, vcc
	v_rsq_f32_e32 v0, v0
	v_pk_mul_f32 v[18:19], v[4:5], v[18:19]
	v_pk_mul_f32 v[20:21], v[6:7], v[20:21]
	v_cvt_pk_bf16_f32 v18, v18, v19
	v_cvt_pk_bf16_f32 v19, v20, v21
	global_store_dwordx4 v[36:37], v[16:19], off
	s_nop 1
	v_mul_f32_e32 v16, 0x45800000, v0
	v_cndmask_b32_e32 v0, v0, v16, vcc
	v_pk_mul_f32 v[16:17], v[0:1], v[48:49] op_sel_hi:[0,1]
	v_pk_mul_f32 v[18:19], v[0:1], v[44:45] op_sel_hi:[0,1]
	v_pk_mul_f32 v[16:17], v[8:9], v[16:17]
	v_pk_mul_f32 v[18:19], v[10:11], v[18:19]
	v_cvt_pk_bf16_f32 v16, v16, v17
	v_cvt_pk_bf16_f32 v17, v18, v19
	v_pk_mul_f32 v[18:19], v[0:1], v[42:43] op_sel_hi:[0,1]
	v_pk_mul_f32 v[20:21], v[0:1], v[38:39] op_sel_hi:[0,1]
	v_pk_mul_f32 v[18:19], v[4:5], v[18:19]
	v_pk_mul_f32 v[20:21], v[6:7], v[20:21]
	v_or_b32_e32 v0, 16, v52
	v_cvt_pk_bf16_f32 v18, v18, v19
	v_cvt_pk_bf16_f32 v19, v20, v21
	v_lshl_add_u64 v[20:21], v[12:13], 0, v[2:3]
	v_lshl_add_u32 v2, v0, 7, v53
	global_store_dwordx4 v[20:21], v[16:19], off
	ds_read_b128 v[20:23], v2 offset:51200
	v_lshlrev_b32_e32 v2, 11, v0
	v_lshl_add_u32 v0, v54, 7, v53
	ds_read_b128 v[26:29], v0 offset:51200
	s_waitcnt lgkmcnt(1)
; __device__ __forceinline__ unsigned cvtpk_s(float lo,float hi){f32x2_t v={lo,hi};bf16x2_t b=__builtin_convertvector(v,bf16x2_t);return __builtin_bit_cast(unsigned,b);}
; template<int THRL> __device__ __forceinline__ void attn_unit(int b,int h,int qb,const bf16*Q,const bf16*__restrict__ K,const bf16*__restrict__ V,bf16*O,const float*__restrict__ F2g,const float*__restrict__ gain,float qkb,char*shm){
;     ...
;     for(int i=0;i<4;++i){const int row=i*8+(lane>>3),ch=lane&7; const u32x4 v=*(const u32x4*)(stg+row*64+ch*8);
;       float x[8];
;       #pragma unroll
;       for(int e=0;e<4;++e){ x[2*e]=__uint_as_float(v[e]<<16); x[2*e+1]=__uint_as_float(v[e]&0xffff0000u); }
;       float ss=0.f;
;       #pragma unroll
;       for(int e=0;e<8;++e)ss+=x[e]*x[e];
;       ss+=__int_as_float(__builtin_amdgcn_ds_bpermute((lane^1)<<2,__float_as_int(ss))); ss+=__int_as_float(__builtin_amdgcn_ds_bpermute((lane^2)<<2,__float_as_int(ss))); ss+=__int_as_float(__builtin_amdgcn_ds_bpermute((lane^4)<<2,__float_as_int(ss)));
;       const float rs=rsqrtf(ss*(1.0f/64.0f)+1e-6f);
;       u32x4 w; w[0]=cvtpk_s(x[0]*rs*g0[0],x[1]*rs*g0[1]); w[1]=cvtpk_s(x[2]*rs*g0[2],x[3]*rs*g0[3]); w[2]=cvtpk_s(x[4]*rs*g1[0],x[5]*rs*g1[1]); w[3]=cvtpk_s(x[6]*rs*g1[2],x[7]*rs*g1[3]);
;       ATTN_STORE16(Ow+(long)row*DO+ch*8,w);} }
;   asm volatile("s_waitcnt lgkmcnt(0)\n\ts_barrier":::"memory");
	v_lshlrev_b32_e32 v36, 16, v20
	v_and_b32_e32 v37, 0xffff0000, v20
	v_lshlrev_b32_e32 v16, 16, v23
	s_waitcnt lgkmcnt(0)
	v_lshlrev_b32_e32 v50, 16, v26
	v_and_b32_e32 v51, 0xffff0000, v26
	v_and_b32_e32 v17, 0xffff0000, v23
	v_lshlrev_b32_e32 v18, 16, v22
	v_and_b32_e32 v19, 0xffff0000, v22
	v_lshlrev_b32_e32 v22, 16, v21
	v_and_b32_e32 v23, 0xffff0000, v21
	v_pk_mul_f32 v[38:39], v[36:37], v[36:37]
	v_lshlrev_b32_e32 v46, 16, v27
	v_and_b32_e32 v47, 0xffff0000, v27
	v_pk_mul_f32 v[26:27], v[50:51], v[50:51]
	v_pk_mul_f32 v[34:35], v[22:23], v[22:23]
	v_pk_mul_f32 v[48:49], v[46:47], v[46:47]
	v_mov_b32_e32 v52, v26
	v_mov_b32_e32 v53, v38
	v_mov_b32_e32 v38, v27
	v_lshlrev_b32_e32 v44, 16, v28
	v_and_b32_e32 v45, 0xffff0000, v28
	v_pk_add_f32 v[26:27], v[52:53], v[38:39]
	v_mov_b32_e32 v38, v48
	v_mov_b32_e32 v39, v34
	v_pk_mul_f32 v[32:33], v[18:19], v[18:19]
	v_lshlrev_b32_e32 v40, 16, v29
	v_and_b32_e32 v41, 0xffff0000, v29
	v_pk_mul_f32 v[28:29], v[44:45], v[44:45]
	v_pk_add_f32 v[26:27], v[38:39], v[26:27]
	v_mov_b32_e32 v34, v49
	v_pk_add_f32 v[26:27], v[34:35], v[26:27]
	v_mov_b32_e32 v34, v28
	v_mov_b32_e32 v35, v32
	v_pk_mul_f32 v[30:31], v[16:17], v[16:17]
	v_pk_mul_f32 v[42:43], v[40:41], v[40:41]
	v_pk_add_f32 v[26:27], v[34:35], v[26:27]
	v_mov_b32_e32 v32, v29
	v_pk_add_f32 v[26:27], v[32:33], v[26:27]
	v_mov_b32_e32 v28, v42
	v_mov_b32_e32 v29, v30
	v_pk_add_f32 v[26:27], v[28:29], v[26:27]
	v_mov_b32_e32 v30, v43
	v_pk_add_f32 v[26:27], v[30:31], v[26:27]
	ds_bpermute_b32 v29, v25, v27
	ds_bpermute_b32 v28, v25, v26
	v_lshl_add_u64 v[20:21], v[12:13], 0, v[2:3]
	s_waitcnt lgkmcnt(0)
	v_pk_add_f32 v[26:27], v[26:27], v[28:29]
	ds_bpermute_b32 v25, v24, v27
	ds_bpermute_b32 v24, v24, v26
	s_waitcnt lgkmcnt(0)
	v_pk_add_f32 v[24:25], v[26:27], v[24:25]
	ds_bpermute_b32 v27, v1, v25
	ds_bpermute_b32 v26, v1, v24
	s_waitcnt lgkmcnt(0)
	v_pk_add_f32 v[0:1], v[24:25], v[26:27]
	s_nop 0
	v_pk_fma_f32 v[0:1], v[0:1], s[96:97], v[14:15] op_sel_hi:[1,0,0]
	s_nop 0
	v_mul_f32_e32 v2, 0x4b800000, v1
	v_cmp_gt_f32_e64 s[0:1], s83, v1
	v_cmp_gt_f32_e32 vcc, s83, v0
	s_nop 0
	v_cndmask_b32_e64 v1, v1, v2, s[0:1]
	v_rsq_f32_e32 v1, v1
	s_nop 0
	v_mul_f32_e32 v2, 0x45800000, v1
	v_cndmask_b32_e64 v2, v1, v2, s[0:1]
	v_pk_mul_f32 v[14:15], v[2:3], v[36:37] op_sel_hi:[0,1]
	v_mul_f32_e32 v1, 0x4b800000, v0
	v_pk_mul_f32 v[14:15], v[8:9], v[14:15]
	v_cndmask_b32_e32 v0, v0, v1, vcc
	v_cvt_pk_bf16_f32 v24, v14, v15
	v_pk_mul_f32 v[14:15], v[2:3], v[22:23] op_sel_hi:[0,1]
	v_rsq_f32_e32 v0, v0
	v_pk_mul_f32 v[14:15], v[10:11], v[14:15]
	s_mov_b64 s[0:1], 0
	v_cvt_pk_bf16_f32 v25, v14, v15
	v_pk_mul_f32 v[14:15], v[2:3], v[18:19] op_sel_hi:[0,1]
	v_pk_mul_f32 v[14:15], v[4:5], v[14:15]
	v_mul_f32_e32 v1, 0x45800000, v0
	v_cvt_pk_bf16_f32 v26, v14, v15
	v_pk_mul_f32 v[14:15], v[2:3], v[16:17] op_sel_hi:[0,1]
	v_pk_mul_f32 v[14:15], v[6:7], v[14:15]
	v_cndmask_b32_e32 v0, v0, v1, vcc
	v_cvt_pk_bf16_f32 v27, v14, v15
	v_pk_mul_f32 v[14:15], v[0:1], v[50:51] op_sel_hi:[0,1]
	v_pk_mul_f32 v[8:9], v[8:9], v[14:15]
	v_pk_mul_f32 v[14:15], v[0:1], v[46:47] op_sel_hi:[0,1]
	v_pk_mul_f32 v[10:11], v[10:11], v[14:15]
	v_cvt_pk_bf16_f32 v8, v8, v9
	v_cvt_pk_bf16_f32 v9, v10, v11
	v_pk_mul_f32 v[10:11], v[0:1], v[44:45] op_sel_hi:[0,1]
	v_pk_mul_f32 v[0:1], v[0:1], v[40:41] op_sel_hi:[0,1]
	v_pk_mul_f32 v[4:5], v[4:5], v[10:11]
	v_pk_mul_f32 v[0:1], v[6:7], v[0:1]
	v_lshlrev_b32_e32 v2, 11, v54
	v_cvt_pk_bf16_f32 v10, v4, v5
	v_cvt_pk_bf16_f32 v11, v0, v1
	v_lshl_add_u64 v[0:1], v[12:13], 0, v[2:3]
	global_store_dwordx4 v[20:21], v[24:27], off
	global_store_dwordx4 v[0:1], v[8:11], off
	s_waitcnt lgkmcnt(0)
	s_barrier

; __global__ void __launch_bounds__(NWAVES * 64, 2) mega_fwd(Args args) {
;     ...
;             for (int pa_ = 0; pa_ <= PROBE_ATT2; ++pa_) for (;;) {
;                 if (F.tid == 0) QS[0] = (int)__hip_atomic_fetch_add(F.ctl + CW_Q + 64 * F.l + 4 * pa_, 1u, __ATOMIC_RELAXED, __HIP_MEMORY_SCOPE_AGENT);
;                 __syncthreads();
;                 const int idx = __builtin_amdgcn_readfirstlane(QS[0]);
;                 __syncthreads();
;                 if (idx >= ((QMODE >= 2) ? 512 : 512 + 2560)) break;
.LBB0_2753:
	s_and_saveexec_b64 s[0:1], s[2:3]
	s_cbranch_execz .LBB0_2757
	s_mov_b64 s[24:25], exec
	v_mbcnt_lo_u32_b32 v0, s24, 0
	v_mbcnt_hi_u32_b32 v1, s25, v0
	v_cmp_eq_u32_e32 vcc, 0, v1
	s_and_saveexec_b64 s[4:5], vcc
	s_cbranch_execz .LBB0_2756
	s_bcnt1_i32_b64 s24, s[24:25]
	v_mov_b32_e32 v0, s24
	s_waitcnt vmcnt(0)
	v_mov_b32_e32 v2, v200

; __global__ void __launch_bounds__(NWAVES * 64, 2) mega_fwd(Args args) {
;     ...
;             } else if (QMODE >= 3) {
;                 for (;;) {
;                     if (F.tid == 0) QS[0] = (int)__hip_atomic_fetch_add(F.ctl + CW_Q + 64 * F.l + 32, 1u, __ATOMIC_RELAXED, __HIP_MEMORY_SCOPE_AGENT);
;                     __syncthreads();
;                     const int j = __builtin_amdgcn_readfirstlane(QS[0]);
.LBB0_2845:
	s_mov_b64 s[26:27], exec
	v_cmp_eq_u32_e32 vcc, 0, v130
	s_and_b64 exec, exec, vcc
	s_cbranch_execz .Lmy_s4w_done
	s_add_u32 s0, s10, s12
	s_addc_u32 s1, s11, s13
	s_add_u32 s24, s0, 0x9080
	s_addc_u32 s25, s1, 0
	v_mov_b32_e32 v247, 1
	global_atomic_add v246, v3, v247, s[24:25] sc0
	s_add_u32 s28, s10, 0xb000
	s_addc_u32 s29, s11, 0
	s_add_i32 s30, s8, 1
	s_lshl_b32 s30, s30, 8
	s_mov_b32 s32, 0
	v_mov_b32_e32 v0, 0

; __global__ void __launch_bounds__(NWAVES * 64, 2) mega_fwd(Args args) {
;     ...
;                 for (;;) {
;                     if (F.tid == 0) QS[0] = (int)__hip_atomic_fetch_add(F.ctl + CW_Q + 64 * F.l + 32, 1u, __ATOMIC_RELAXED, __HIP_MEMORY_SCOPE_AGENT);
;                     __syncthreads();
;                     const int j = __builtin_amdgcn_readfirstlane(QS[0]);
;                     __syncthreads();
.LBB0_2846:
	s_mov_b64 s[4:5], exec
	v_mbcnt_lo_u32_b32 v0, s4, 0
	v_mbcnt_hi_u32_b32 v1, s5, v0
	v_cmp_eq_u32_e32 vcc, 0, v1
	s_and_saveexec_b64 s[2:3], vcc
	s_cbranch_execz .LBB0_2848
	s_bcnt1_i32_b64 s4, s[4:5]
	v_mov_b32_e32 v0, s4
	s_waitcnt vmcnt(0)
	v_mov_b32_e32 v2, v246
	global_atomic_add v246, v3, v0, s[24:25] sc0
.LBB0_2848:
	s_or_b64 exec, exec, s[2:3]
	s_nop 0
	v_readfirstlane_b32 s2, v2
	s_nop 1
	v_add_u32_e32 v0, s2, v1
	v_mov_b32_e32 v1, s17
	ds_write_b32 v1, v0
